# MLA online softmax: exponentials taken against the carried max first; the exact row-max pass (max tree, exchange, rescale, recomputed scores) only runs when a tile row sum exceeds 2^14
# speedup vs baseline: 1.0250x; 1.0034x over previous
.LBB0_457:
	s_mov_b32 s101, 0
	s_lshl_b32 s5, s36, 8
	s_and_b32 s37, s5, 0xf00
	s_ashr_i32 s4, s36, 7
	s_xor_b32 s7, s37, 0x1f00
	v_readlane_b32 s5, v239, 14
	s_mov_b64 s[18:19], s[78:79]
	s_waitcnt vmcnt(0)
	v_mov_b32_e32 v66, v0
	s_add_i32 s41, s7, s5
	s_ashr_i32 s5, s4, 31
	s_lshl_b64 s[10:11], s[4:5], 13
	v_and_or_b32 v166, v66, 31, s41
	s_bfe_u32 s6, s36, 0x30004
	v_lshl_add_u64 v[174:175], s[10:11], 0, v[166:167]
	s_waitcnt vmcnt(0) lgkmcnt(0)
	v_mov_b64_e32 v[2:3], s[0:1]
	s_movk_i32 s12, 0xc00
	v_mad_u64_u32 v[2:3], s[8:9], v174, s12, v[2:3]
	s_mul_i32 s40, s6, 0xc0
	v_bfe_u32 v1, v66, 5, 1
	v_mad_i32_i24 v3, v175, s12, v3
	s_lshl_b32 s84, s40, 1
	v_lshl_add_u64 v[2:3], v[2:3], 0, s[84:85]
	v_lshlrev_b32_e32 v172, 4, v1
	v_mov_b32_e32 v173, v167
	v_lshl_add_u64 v[48:49], v[2:3], 0, v[172:173]
	v_lshlrev_b64 v[6:7], 8, v[174:175]
	global_load_dwordx4 v[16:19], v[48:49], off offset:256
	global_load_dwordx4 v[2:5], v[48:49], off offset:320
	v_lshl_add_u64 v[6:7], s[2:3], 0, v[6:7]
	v_lshlrev_b32_e32 v14, 5, v1
	v_mov_b32_e32 v15, v167
	v_lshl_add_u64 v[40:41], v[6:7], 0, v[14:15]
	global_load_dwordx4 v[20:23], v[40:41], off offset:128
	global_load_dwordx4 v[6:9], v[40:41], off offset:144
	global_load_dwordx4 v[24:27], v[40:41], off
	global_load_dwordx4 v[10:13], v[40:41], off offset:16
	v_lshlrev_b32_e32 v1, 2, v66
	v_lshrrev_b32_e32 v15, 1, v66
	v_and_b32_e32 v28, 3, v66
	v_and_b32_e32 v15, 12, v15
	v_and_b32_e32 v69, 16, v1
	v_or3_b32 v15, v15, v28, v69
	global_load_dwordx4 v[28:31], v[40:41], off offset:80
	global_load_dwordx4 v[32:35], v[40:41], off offset:64
	global_load_dwordx4 v[36:39], v[40:41], off offset:208
	s_nop 0
	global_load_dwordx4 v[40:43], v[40:41], off offset:192
	s_nop 0
	global_load_dwordx4 v[98:101], v[48:49], off
	global_load_dwordx4 v[102:105], v[48:49], off offset:32
	global_load_dwordx4 v[106:109], v[48:49], off offset:64
	global_load_dwordx4 v[110:113], v[48:49], off offset:96
	global_load_dwordx4 v[114:117], v[48:49], off offset:128
	global_load_dwordx4 v[118:121], v[48:49], off offset:160
	global_load_dwordx4 v[122:125], v[48:49], off offset:192
	global_load_dwordx4 v[126:129], v[48:49], off offset:224
	global_load_dwordx4 v[44:47], v[48:49], off offset:288
	s_nop 0
	global_load_dwordx4 v[48:51], v[48:49], off offset:352
	v_lshlrev_b32_e32 v67, 6, v66
	v_lshlrev_b32_e32 v68, 3, v66
	s_lshl_b32 s21, s6, 22
	s_lshl_b32 s20, s6, 8
	s_add_i32 s22, s7, 0x100
	v_and_b32_e32 v70, 0x78, v68
	s_mov_b32 s7, 0x7ffffc00
	s_lshl_b64 s[8:9], s[4:5], 24
	v_and_or_b32 v1, v67, s7, v70
	s_mov_b32 s23, 0x7fffc000
	v_lshlrev_b32_e32 v1, 1, v1
	s_barrier
	s_mov_b32 s47, 0
	v_mov_b32_e32 v207, 0xf149f2ca
	v_mov_b32_e32 v205, 0
	s_mov_b32 s45, 63
	s_waitcnt vmcnt(19)
	v_lshlrev_b32_e32 v52, 16, v16
	v_and_b32_e32 v53, 0xffff0000, v16
	s_waitcnt vmcnt(18)
	v_lshlrev_b32_e32 v54, 16, v2
	v_and_b32_e32 v55, 0xffff0000, v2
	v_lshlrev_b32_e32 v16, 16, v17
	v_and_b32_e32 v17, 0xffff0000, v17
	v_lshlrev_b32_e32 v2, 16, v3
	v_and_b32_e32 v3, 0xffff0000, v3
	v_lshlrev_b32_e32 v56, 16, v18
	v_and_b32_e32 v57, 0xffff0000, v18
	v_lshlrev_b32_e32 v58, 16, v4
	v_and_b32_e32 v59, 0xffff0000, v4
	s_waitcnt vmcnt(17)
	v_pk_mul_f32 v[62:63], v[22:23], v[2:3]
	v_pk_mul_f32 v[22:23], v[22:23], v[16:17]
	s_waitcnt vmcnt(16)
	v_pk_mul_f32 v[64:65], v[6:7], v[58:59]
	v_pk_mul_f32 v[6:7], v[6:7], v[56:57]
	s_waitcnt vmcnt(15)
	v_pk_fma_f32 v[2:3], v[26:27], v[2:3], v[22:23]
	s_waitcnt vmcnt(14)
	v_pk_fma_f32 v[22:23], v[10:11], v[56:57], v[64:65] neg_lo:[0,0,1] neg_hi:[0,0,1]
	v_pk_fma_f32 v[6:7], v[10:11], v[58:59], v[6:7]
	v_add_u32_e32 v10, 0x8000, v67
	v_and_or_b32 v10, v10, s7, v70
	s_add_u32 s7, s28, s8
	v_lshlrev_b32_e32 v173, 1, v10
	v_lshlrev_b32_e32 v10, 11, v66
	v_and_b32_e32 v11, 56, v68
	s_addc_u32 s13, s29, s9
	s_lshl_b32 s42, s6, 7
	v_cvt_pk_bf16_f32 v132, v22, v23
	v_and_or_b32 v22, v10, s23, v11
	s_add_u32 s12, s7, s20
	v_lshlrev_b32_e32 v178, 1, v22
	s_addc_u32 s13, s13, 0
	v_mov_b32_e32 v22, v1
	global_load_dwordx4 v[134:137], v22, s[12:13]
	v_pk_fma_f32 v[16:17], v[26:27], v[16:17], v[62:63] neg_lo:[0,0,1] neg_hi:[0,0,1]
	s_lshl_b64 s[6:7], s[4:5], 20
	v_cvt_pk_bf16_f32 v131, v16, v17
	v_lshlrev_b32_e32 v17, 4, v66
	s_add_u32 s14, s30, s6
	v_ashrrev_i32_e32 v16, 3, v66
	v_and_b32_e32 v176, 0x70, v17
	s_addc_u32 s15, s31, s7
	v_mov_b32_e32 v22, v173
	v_lshl_or_b32 v177, v16, 7, v176
	s_add_u32 s16, s34, s21
	global_load_dwordx4 v[138:141], v22, s[12:13]
	s_addc_u32 s17, s35, 0
	s_lshl_b64 s[4:5], s[4:5], 14
	v_mov_b32_e32 v22, v177
	s_add_u32 s16, s16, s4
	v_add_u32_e32 v10, 0x100000, v10
	global_load_dwordx4 v[142:145], v22, s[14:15]
	s_addc_u32 s17, s17, s5
	v_mov_b32_e32 v22, v178
	v_and_or_b32 v10, v10, s23, v11
	global_load_dwordx4 v[154:157], v22, s[16:17]
	v_lshlrev_b32_e32 v179, 1, v10
	v_mov_b32_e32 v10, v179
	global_load_dwordx4 v[158:161], v10, s[16:17]
	v_lshlrev_b32_e32 v18, 16, v19
	v_and_b32_e32 v19, 0xffff0000, v19
	v_lshlrev_b32_e32 v4, 16, v5
	v_and_b32_e32 v5, 0xffff0000, v5
	v_pk_mul_f32 v[10:11], v[8:9], v[4:5]
	v_pk_mul_f32 v[8:9], v[8:9], v[18:19]
	v_cvt_pk_bf16_f32 v147, v2, v3
	v_pk_fma_f32 v[4:5], v[12:13], v[4:5], v[8:9]
	v_cvt_pk_bf16_f32 v148, v6, v7
	v_cvt_pk_bf16_f32 v149, v4, v5
	s_waitcnt vmcnt(5)
	v_lshlrev_b32_e32 v4, 16, v48
	v_and_b32_e32 v5, 0xffff0000, v48
	v_lshlrev_b32_e32 v2, 16, v44
	v_and_b32_e32 v3, 0xffff0000, v44
	v_pk_mul_f32 v[6:7], v[40:41], v[4:5]
	s_movk_i32 s23, 0x1a0
	v_pk_fma_f32 v[6:7], v[32:33], v[2:3], v[6:7] neg_lo:[0,0,1] neg_hi:[0,0,1]
	v_pk_mul_f32 v[2:3], v[40:41], v[2:3]
	v_and_b32_e32 v180, 0xf0, v17
	v_pk_fma_f32 v[2:3], v[32:33], v[4:5], v[2:3]
	v_cvt_pk_bf16_f32 v150, v6, v7
	v_cvt_pk_bf16_f32 v162, v2, v3
	v_ashrrev_i32_e32 v2, 4, v66
	v_mul_lo_u32 v181, v2, s23
	v_add_u32_e32 v3, 0, v181
	v_and_b32_e32 v182, 16, v2
	v_lshlrev_b32_e32 v6, 16, v49
	v_and_b32_e32 v7, 0xffff0000, v49
	v_add3_u32 v2, v3, v182, v180
	v_lshlrev_b32_e32 v4, 16, v45
	v_and_b32_e32 v5, 0xffff0000, v45
	v_pk_mul_f32 v[8:9], v[42:43], v[6:7]
	v_and_b32_e32 v185, 16, v16
	v_pk_fma_f32 v[8:9], v[34:35], v[4:5], v[8:9] neg_lo:[0,0,1] neg_hi:[0,0,1]
	v_pk_mul_f32 v[4:5], v[42:43], v[4:5]
	s_lshr_b32 s43, s22, 6
	v_pk_fma_f32 v[4:5], v[34:35], v[6:7], v[4:5]
	s_or_b32 s44, s41, 31
	v_cvt_pk_bf16_f32 v163, v4, v5
	v_pk_fma_f32 v[10:11], v[12:13], v[18:19], v[10:11] neg_lo:[0,0,1] neg_hi:[0,0,1]
	v_cvt_pk_bf16_f32 v151, v8, v9
	v_lshlrev_b32_e32 v8, 16, v50
	v_and_b32_e32 v9, 0xffff0000, v50
	s_add_u32 s4, s21, s4
	v_cvt_pk_bf16_f32 v133, v10, v11
	v_lshlrev_b32_e32 v6, 16, v46
	v_and_b32_e32 v7, 0xffff0000, v46
	v_pk_mul_f32 v[10:11], v[36:37], v[8:9]
	s_addc_u32 s5, 0, s5
	v_pk_fma_f32 v[10:11], v[28:29], v[6:7], v[10:11] neg_lo:[0,0,1] neg_hi:[0,0,1]
	s_waitcnt vmcnt(4)
	ds_write_b128 v2, v[134:137]
	v_add_u32_e32 v2, 0x200, v66
	v_ashrrev_i32_e32 v3, 4, v2
	v_mul_lo_u32 v183, v3, s23
	v_add_u32_e32 v4, 0, v183
	v_and_b32_e32 v184, 16, v3
	v_add3_u32 v3, v4, v184, v180
	v_lshlrev_b32_e32 v4, 8, v16
	v_ashrrev_i32_e32 v2, 3, v2
	v_and_b32_e32 v202, 16, v2
	s_add_u32 s4, s4, 0x10400080
	v_cvt_pk_bf16_f32 v152, v10, v11
	v_pk_mul_f32 v[6:7], v[36:37], v[6:7]
	s_waitcnt vmcnt(3)
	ds_write_b128 v3, v[138:141]
	v_mul_lo_u32 v3, v16, s23
	v_add3_u32 v3, 0, v3, v185
	v_add_u32_e32 v199, v3, v176
	s_movk_i32 s23, 0xa0
	v_sub_u32_e32 v3, v3, v4
	v_add_u32_e32 v3, v3, v176
	v_mul_lo_u32 v201, v2, s23
	s_waitcnt vmcnt(2)
	ds_write_b128 v199, v[142:145] offset:256
	v_lshlrev_b32_e32 v10, 16, v51
	v_and_b32_e32 v11, 0xffff0000, v51
	s_addc_u32 s5, s5, 0
	s_waitcnt vmcnt(1)
	ds_write_b128 v3, v[154:157] offset:53248
	v_add_u32_e32 v3, 0, v201
	v_add3_u32 v2, v3, v202, v176
	v_pk_fma_f32 v[6:7], v[28:29], v[8:9], v[6:7]
	v_lshlrev_b32_e32 v8, 16, v47
	v_and_b32_e32 v9, 0xffff0000, v47
	v_pk_mul_f32 v[12:13], v[38:39], v[10:11]
	s_waitcnt vmcnt(0)
	ds_write_b128 v2, v[158:161] offset:53248
	v_mul_u32_u24_e32 v2, 0x1a0, v15
	s_add_u32 s6, s6, 0xae02000
	v_pk_mul_f32 v[60:61], v[20:21], v[54:55]
	v_pk_mul_f32 v[20:21], v[20:21], v[52:53]
	v_pk_fma_f32 v[12:13], v[30:31], v[8:9], v[12:13] neg_lo:[0,0,1] neg_hi:[0,0,1]
	v_pk_mul_f32 v[8:9], v[38:39], v[8:9]
	v_add3_u32 v2, 0, v2, v69
	v_lshlrev_b32_e32 v3, 8, v15
	s_addc_u32 s7, s7, 0
	s_or_b32 s8, s8, s20
	v_pk_fma_f32 v[52:53], v[24:25], v[52:53], v[60:61] neg_lo:[0,0,1] neg_hi:[0,0,1]
	v_pk_fma_f32 v[20:21], v[24:25], v[54:55], v[20:21]
	v_pk_fma_f32 v[8:9], v[30:31], v[10:11], v[8:9]
	v_add_u32_e32 v203, v2, v172
	v_sub_u32_e32 v2, v2, v3
	s_add_u32 s8, s8, 0xe420000
	v_mov_b32_e32 v18, v167
	v_mov_b32_e32 v19, v167
	v_mov_b32_e32 v32, v167
	v_mov_b32_e32 v33, v167
	v_cvt_pk_bf16_f32 v130, v52, v53
	v_cvt_pk_bf16_f32 v146, v20, v21
	v_cvt_pk_bf16_f32 v153, v12, v13
	v_cvt_pk_bf16_f32 v164, v6, v7
	v_cvt_pk_bf16_f32 v165, v8, v9
	v_mul_lo_u32 v200, v16, s23
	v_add_u32_e32 v204, v2, v14
	s_addc_u32 s9, s9, 0
	v_mov_b32_e32 v20, v167
	v_mov_b32_e32 v21, v167
	v_mov_b32_e32 v22, v167
	v_mov_b32_e32 v23, v167
	v_mov_b32_e32 v24, v167
	v_mov_b32_e32 v25, v167
	v_mov_b32_e32 v26, v167
	v_mov_b32_e32 v27, v167
	v_mov_b32_e32 v28, v167
	v_mov_b32_e32 v29, v167
	v_mov_b32_e32 v30, v167
	v_mov_b32_e32 v31, v167
	v_mov_b64_e32 v[48:49], v[32:33]
	v_mov_b64_e32 v[64:65], v[32:33]
	v_mov_b64_e32 v[2:3], v[18:19]
	s_mov_b64 s[20:21], s[8:9]
	s_mov_b64 s[22:23], s[6:7]
	s_mov_b64 s[24:25], s[4:5]
	v_mov_b64_e32 v[46:47], v[30:31]
	v_mov_b64_e32 v[44:45], v[28:29]
	v_mov_b64_e32 v[42:43], v[26:27]
	v_mov_b64_e32 v[40:41], v[24:25]
	v_mov_b64_e32 v[38:39], v[22:23]
	v_mov_b64_e32 v[36:37], v[20:21]
	v_mov_b64_e32 v[34:35], v[18:19]
	v_mov_b64_e32 v[62:63], v[30:31]
	v_mov_b64_e32 v[60:61], v[28:29]
	v_mov_b64_e32 v[58:59], v[26:27]
	v_mov_b64_e32 v[56:57], v[24:25]
	v_mov_b64_e32 v[54:55], v[22:23]
	v_mov_b64_e32 v[52:53], v[20:21]
	v_mov_b64_e32 v[50:51], v[18:19]
	v_mov_b64_e32 v[4:5], v[20:21]
	v_mov_b64_e32 v[6:7], v[22:23]
	v_mov_b64_e32 v[8:9], v[24:25]
	v_mov_b64_e32 v[10:11], v[26:27]
	v_mov_b64_e32 v[12:13], v[28:29]
	v_mov_b64_e32 v[14:15], v[30:31]
	v_mov_b64_e32 v[16:17], v[32:33]
	s_waitcnt lgkmcnt(0)
	s_barrier
	v_and_b32_e32 v237, 64, v192
	v_xor_b32_e32 v236, 32, v192
	v_add_u32_e32 v237, 64, v237
	v_cmp_lt_i32_e32 vcc, v236, v237
	s_nop 1
	v_cndmask_b32_e32 v236, v192, v236, vcc
	v_lshlrev_b32_e32 v236, 2, v236

.LBB0_463:
	s_nop 9
	s_cmp_eq_u32 s101, 0
	s_cbranch_scc0 .Lmy_force_a
	v_mov_b32_e32 v206, v207
	s_branch .LBB0_465
.Lmy_force_a:
	v_max3_f32 v206, v82, v66, s90
	v_max_f32_e32 v208, v83, v67
	v_max3_f32 v206, v206, v84, v68
	v_max3_f32 v208, v208, v85, v69
	v_max3_f32 v206, v206, v86, v70
	v_max3_f32 v208, v208, v87, v71
	v_max3_f32 v206, v206, v88, v72
	v_max3_f32 v208, v208, v89, v73
	v_max3_f32 v206, v206, v90, v74
	v_max3_f32 v208, v208, v91, v75
	v_max3_f32 v206, v206, v92, v76
	v_max3_f32 v208, v208, v93, v77
	v_max3_f32 v206, v206, v94, v78
	v_max3_f32 v208, v208, v95, v79
	v_max3_f32 v206, v206, v96, v80
	v_max3_f32 v208, v208, v97, v81
	v_max_f32_e32 v206, v206, v208
	v_add_f32_e32 v208, 0x4299999a, v207
	v_cmp_gt_f32_e32 vcc, v206, v208
	s_cbranch_vccnz .Lmy_lazy_a
	v_mov_b32_e32 v206, v207
	s_branch .LBB0_465

.LBB0_465:
	s_mov_b32 s100, 0x3dd53b94
	v_mul_f32_e32 v208, 0xbdd53b94, v206
	s_nop 0
	v_pk_fma_f32 v[82:83], v[82:83], s[100:101], v[208:209] op_sel_hi:[1,0,0]
	v_pk_fma_f32 v[66:67], v[66:67], s[100:101], v[208:209] op_sel_hi:[1,0,0]
	v_exp_f32_e32 v82, v82
	v_exp_f32_e32 v83, v83
	v_pk_fma_f32 v[84:85], v[84:85], s[100:101], v[208:209] op_sel_hi:[1,0,0]
	v_exp_f32_e32 v210, v66
	v_exp_f32_e32 v211, v67
	v_pk_fma_f32 v[68:69], v[68:69], s[100:101], v[208:209] op_sel_hi:[1,0,0]
	v_exp_f32_e32 v84, v84
	v_exp_f32_e32 v85, v85
	v_pk_fma_f32 v[86:87], v[86:87], s[100:101], v[208:209] op_sel_hi:[1,0,0]
	v_pk_add_f32 v[66:67], v[82:83], v[210:211]
	v_exp_f32_e32 v212, v68
	v_exp_f32_e32 v213, v69
	v_pk_fma_f32 v[70:71], v[70:71], s[100:101], v[208:209] op_sel_hi:[1,0,0]
	v_exp_f32_e32 v86, v86
	v_exp_f32_e32 v87, v87
	v_pk_fma_f32 v[88:89], v[88:89], s[100:101], v[208:209] op_sel_hi:[1,0,0]
	v_pk_add_f32 v[68:69], v[84:85], v[212:213]
	v_exp_f32_e32 v214, v70
	v_exp_f32_e32 v215, v71
	v_pk_fma_f32 v[72:73], v[72:73], s[100:101], v[208:209] op_sel_hi:[1,0,0]
	v_exp_f32_e32 v88, v88
	v_exp_f32_e32 v89, v89
	v_pk_fma_f32 v[90:91], v[90:91], s[100:101], v[208:209] op_sel_hi:[1,0,0]
	v_pk_add_f32 v[70:71], v[86:87], v[214:215]
	v_exp_f32_e32 v216, v72
	v_exp_f32_e32 v217, v73
	v_pk_fma_f32 v[74:75], v[74:75], s[100:101], v[208:209] op_sel_hi:[1,0,0]
	v_exp_f32_e32 v90, v90
	v_exp_f32_e32 v91, v91
	v_pk_fma_f32 v[92:93], v[92:93], s[100:101], v[208:209] op_sel_hi:[1,0,0]
	v_pk_add_f32 v[72:73], v[88:89], v[216:217]
	v_exp_f32_e32 v218, v74
	v_exp_f32_e32 v219, v75
	v_pk_fma_f32 v[76:77], v[76:77], s[100:101], v[208:209] op_sel_hi:[1,0,0]
	v_exp_f32_e32 v92, v92
	v_exp_f32_e32 v93, v93
	v_pk_fma_f32 v[94:95], v[94:95], s[100:101], v[208:209] op_sel_hi:[1,0,0]
	v_pk_add_f32 v[74:75], v[90:91], v[218:219]
	v_exp_f32_e32 v220, v76
	v_exp_f32_e32 v221, v77
	v_pk_fma_f32 v[78:79], v[78:79], s[100:101], v[208:209] op_sel_hi:[1,0,0]
	v_exp_f32_e32 v94, v94
	v_exp_f32_e32 v95, v95
	v_pk_fma_f32 v[96:97], v[96:97], s[100:101], v[208:209] op_sel_hi:[1,0,0]
	v_pk_add_f32 v[76:77], v[92:93], v[220:221]
	v_exp_f32_e32 v222, v78
	v_exp_f32_e32 v223, v79
	v_pk_fma_f32 v[80:81], v[80:81], s[100:101], v[208:209] op_sel_hi:[1,0,0]
	v_exp_f32_e32 v96, v96
	v_exp_f32_e32 v97, v97
	v_pk_add_f32 v[78:79], v[94:95], v[222:223]
	v_exp_f32_e32 v208, v80
	v_exp_f32_e32 v209, v81
	s_nop 0
	v_pk_add_f32 v[80:81], v[96:97], v[208:209]
	v_pk_add_f32 v[66:67], v[66:67], v[68:69]
	v_pk_add_f32 v[70:71], v[70:71], v[72:73]
	v_pk_add_f32 v[74:75], v[74:75], v[76:77]
	v_pk_add_f32 v[78:79], v[78:79], v[80:81]
	v_pk_add_f32 v[66:67], v[66:67], v[70:71]
	v_pk_add_f32 v[74:75], v[74:75], v[78:79]
	v_pk_add_f32 v[66:67], v[66:67], v[74:75]
	v_cvt_pk_bf16_f32 v73, v96, v97
	s_mul_i32 s48, s47, 0x5000
	v_add_f32_e32 v97, v66, v67
	s_nop 0
	v_cmp_nge_f32_e32 vcc, 0x46800000, v97
	s_cbranch_vccz .Lmy_ok_a
	s_cmp_eq_u32 s101, 0
	s_cbranch_scc0 .Lmy_ok_a
	s_mov_b32 s101, 1
	s_branch .LBB0_460
.Lmy_ok_a:
	s_mov_b32 s101, 0
	v_cvt_pk_bf16_f32 v66, v82, v83
	v_cvt_pk_bf16_f32 v67, v84, v85
	v_cvt_pk_bf16_f32 v68, v86, v87
	v_cvt_pk_bf16_f32 v69, v88, v89
	v_cvt_pk_bf16_f32 v70, v90, v91
	v_cvt_pk_bf16_f32 v71, v92, v93
	v_cvt_pk_bf16_f32 v72, v94, v95
	v_add_u32_e32 v90, s48, v204
	ds_read_b128 v[82:85], v90 offset:53248
	ds_read_b128 v[86:89], v90 offset:58368
	v_cvt_pk_bf16_f32 v74, v210, v211
	v_cvt_pk_bf16_f32 v75, v212, v213
	v_cvt_pk_bf16_f32 v76, v214, v215
	v_cvt_pk_bf16_f32 v77, v216, v217
	v_cvt_pk_bf16_f32 v78, v218, v219
	v_cvt_pk_bf16_f32 v79, v220, v221
	v_cvt_pk_bf16_f32 v80, v222, v223
	v_cvt_pk_bf16_f32 v81, v208, v209
	v_add_u32_e32 v91, 0xd000, v90
	s_waitcnt lgkmcnt(1)
	v_mfma_f32_32x32x16_bf16 v[50:65], v[82:85], v[66:69], v[50:65]
	ds_read_b128 v[82:85], v90 offset:63488
	s_waitcnt lgkmcnt(1)
	v_mfma_f32_32x32x16_bf16 v[34:49], v[86:89], v[66:69], v[34:49]
	ds_read_b128 v[86:89], v91 offset:15360
	s_waitcnt lgkmcnt(1)
	v_mfma_f32_32x32x16_bf16 v[18:33], v[82:85], v[66:69], v[18:33]
	ds_read_b128 v[82:85], v90 offset:53264
	s_waitcnt lgkmcnt(1)
	v_mfma_f32_32x32x16_bf16 v[2:17], v[86:89], v[66:69], v[2:17]
	ds_read_b128 v[66:69], v90 offset:58384
	s_waitcnt lgkmcnt(1)
	v_mfma_f32_32x32x16_bf16 v[50:65], v[82:85], v[70:73], v[50:65]
	ds_read_b128 v[82:85], v90 offset:63504
	s_waitcnt lgkmcnt(1)
	v_mfma_f32_32x32x16_bf16 v[34:49], v[66:69], v[70:73], v[34:49]
	ds_read_b128 v[66:69], v91 offset:15376
	s_waitcnt lgkmcnt(1)
	v_mfma_f32_32x32x16_bf16 v[18:33], v[82:85], v[70:73], v[18:33]
	ds_read_b128 v[82:85], v90 offset:53312
	s_waitcnt lgkmcnt(1)
	v_mfma_f32_32x32x16_bf16 v[2:17], v[66:69], v[70:73], v[2:17]
	ds_read_b128 v[66:69], v90 offset:58432
	s_waitcnt lgkmcnt(1)
	v_mfma_f32_32x32x16_bf16 v[50:65], v[82:85], v[74:77], v[50:65]
	ds_read_b128 v[70:73], v90 offset:63552
	s_waitcnt lgkmcnt(1)
	v_mfma_f32_32x32x16_bf16 v[34:49], v[66:69], v[74:77], v[34:49]
	ds_read_b128 v[66:69], v91 offset:15424
	s_waitcnt lgkmcnt(1)
	v_mfma_f32_32x32x16_bf16 v[18:33], v[70:73], v[74:77], v[18:33]
	ds_read_b128 v[70:73], v90 offset:53328
	s_waitcnt lgkmcnt(1)
	v_mfma_f32_32x32x16_bf16 v[2:17], v[66:69], v[74:77], v[2:17]
	ds_read_b128 v[66:69], v90 offset:58448
	s_waitcnt lgkmcnt(1)
	v_mfma_f32_32x32x16_bf16 v[50:65], v[70:73], v[78:81], v[50:65]
	ds_read_b128 v[70:73], v90 offset:63568
	s_waitcnt lgkmcnt(1)
	v_mfma_f32_32x32x16_bf16 v[34:49], v[66:69], v[78:81], v[34:49]
	ds_read_b128 v[66:69], v91 offset:15440
	s_waitcnt lgkmcnt(1)
	v_mfma_f32_32x32x16_bf16 v[18:33], v[70:73], v[78:81], v[18:33]
	s_waitcnt lgkmcnt(0)
	v_mfma_f32_32x32x16_bf16 v[2:17], v[66:69], v[78:81], v[2:17]
	v_add_f32_e32 v205, v97, v205
	s_andn2_b64 vcc, exec, s[26:27]
	s_cbranch_vccz .LBB0_467
	s_branch .LBB0_468

.LBB0_476:
	s_nop 9
	s_cmp_eq_u32 s101, 0
	s_cbranch_scc0 .Lmy_force_b
	v_mov_b32_e32 v207, v208
	s_branch .LBB0_478
.Lmy_force_b:
	v_max3_f32 v207, v82, v66, s90
	v_max_f32_e32 v209, v83, v67
	v_max3_f32 v207, v207, v84, v68
	v_max3_f32 v209, v209, v85, v69
	v_max3_f32 v207, v207, v86, v70
	v_max3_f32 v209, v209, v87, v71
	v_max3_f32 v207, v207, v88, v72
	v_max3_f32 v209, v209, v89, v73
	v_max3_f32 v207, v207, v90, v74
	v_max3_f32 v209, v209, v91, v75
	v_max3_f32 v207, v207, v92, v76
	v_max3_f32 v209, v209, v93, v77
	v_max3_f32 v207, v207, v94, v78
	v_max3_f32 v209, v209, v95, v79
	v_max3_f32 v207, v207, v96, v80
	v_max3_f32 v209, v209, v97, v81
	v_max_f32_e32 v207, v207, v209
	v_add_f32_e32 v209, 0x4299999a, v208
	v_cmp_gt_f32_e32 vcc, v207, v209
	s_cbranch_vccnz .Lmy_lazy_b
	v_mov_b32_e32 v207, v208
	s_branch .LBB0_478

.LBB0_478:
	s_mov_b32 s100, 0x3dd53b94
	v_mul_f32_e32 v208, 0xbdd53b94, v207
	s_nop 0
	v_pk_fma_f32 v[82:83], v[82:83], s[100:101], v[208:209] op_sel_hi:[1,0,0]
	v_pk_fma_f32 v[66:67], v[66:67], s[100:101], v[208:209] op_sel_hi:[1,0,0]
	v_exp_f32_e32 v82, v82
	v_exp_f32_e32 v83, v83
	v_pk_fma_f32 v[84:85], v[84:85], s[100:101], v[208:209] op_sel_hi:[1,0,0]
	v_exp_f32_e32 v210, v66
	v_exp_f32_e32 v211, v67
	v_pk_fma_f32 v[68:69], v[68:69], s[100:101], v[208:209] op_sel_hi:[1,0,0]
	v_exp_f32_e32 v84, v84
	v_exp_f32_e32 v85, v85
	v_pk_fma_f32 v[86:87], v[86:87], s[100:101], v[208:209] op_sel_hi:[1,0,0]
	v_pk_add_f32 v[66:67], v[82:83], v[210:211]
	v_exp_f32_e32 v212, v68
	v_exp_f32_e32 v213, v69
	v_pk_fma_f32 v[70:71], v[70:71], s[100:101], v[208:209] op_sel_hi:[1,0,0]
	v_exp_f32_e32 v86, v86
	v_exp_f32_e32 v87, v87
	v_pk_fma_f32 v[88:89], v[88:89], s[100:101], v[208:209] op_sel_hi:[1,0,0]
	v_pk_add_f32 v[68:69], v[84:85], v[212:213]
	v_exp_f32_e32 v214, v70
	v_exp_f32_e32 v215, v71
	v_pk_fma_f32 v[72:73], v[72:73], s[100:101], v[208:209] op_sel_hi:[1,0,0]
	v_exp_f32_e32 v88, v88
	v_exp_f32_e32 v89, v89
	v_pk_fma_f32 v[90:91], v[90:91], s[100:101], v[208:209] op_sel_hi:[1,0,0]
	v_pk_add_f32 v[70:71], v[86:87], v[214:215]
	v_exp_f32_e32 v216, v72
	v_exp_f32_e32 v217, v73
	v_pk_fma_f32 v[74:75], v[74:75], s[100:101], v[208:209] op_sel_hi:[1,0,0]
	v_exp_f32_e32 v90, v90
	v_exp_f32_e32 v91, v91
	v_pk_fma_f32 v[92:93], v[92:93], s[100:101], v[208:209] op_sel_hi:[1,0,0]
	v_pk_add_f32 v[72:73], v[88:89], v[216:217]
	v_exp_f32_e32 v218, v74
	v_exp_f32_e32 v219, v75
	v_pk_fma_f32 v[76:77], v[76:77], s[100:101], v[208:209] op_sel_hi:[1,0,0]
	v_exp_f32_e32 v92, v92
	v_exp_f32_e32 v93, v93
	v_pk_fma_f32 v[94:95], v[94:95], s[100:101], v[208:209] op_sel_hi:[1,0,0]
	v_pk_add_f32 v[74:75], v[90:91], v[218:219]
	v_exp_f32_e32 v220, v76
	v_exp_f32_e32 v221, v77
	v_pk_fma_f32 v[78:79], v[78:79], s[100:101], v[208:209] op_sel_hi:[1,0,0]
	v_exp_f32_e32 v94, v94
	v_exp_f32_e32 v95, v95
	v_pk_fma_f32 v[96:97], v[96:97], s[100:101], v[208:209] op_sel_hi:[1,0,0]
	v_pk_add_f32 v[76:77], v[92:93], v[220:221]
	v_exp_f32_e32 v222, v78
	v_exp_f32_e32 v223, v79
	v_pk_fma_f32 v[80:81], v[80:81], s[100:101], v[208:209] op_sel_hi:[1,0,0]
	v_exp_f32_e32 v96, v96
	v_exp_f32_e32 v97, v97
	v_pk_add_f32 v[78:79], v[94:95], v[222:223]
	v_exp_f32_e32 v208, v80
	v_exp_f32_e32 v209, v81
	s_nop 0
	v_pk_add_f32 v[80:81], v[96:97], v[208:209]
	v_pk_add_f32 v[66:67], v[66:67], v[68:69]
	v_pk_add_f32 v[70:71], v[70:71], v[72:73]
	v_pk_add_f32 v[74:75], v[74:75], v[76:77]
	v_pk_add_f32 v[78:79], v[78:79], v[80:81]
	v_pk_add_f32 v[66:67], v[66:67], v[70:71]
	v_pk_add_f32 v[74:75], v[74:75], v[78:79]
	v_pk_add_f32 v[66:67], v[66:67], v[74:75]
	v_cvt_pk_bf16_f32 v73, v96, v97
	s_mul_i32 s22, s17, 0x5000
	v_add_f32_e32 v97, v66, v67
	s_nop 0
	v_cmp_nge_f32_e32 vcc, 0x46800000, v97
	s_cbranch_vccz .Lmy_ok_b
	s_cmp_eq_u32 s101, 0
	s_cbranch_scc0 .Lmy_ok_b
	s_mov_b32 s101, 1
	v_mov_b32_e32 v208, v207
	s_branch .LBB0_473
.Lmy_ok_b:
	s_mov_b32 s101, 0
	v_cvt_pk_bf16_f32 v66, v82, v83
	v_cvt_pk_bf16_f32 v67, v84, v85
	v_cvt_pk_bf16_f32 v68, v86, v87
	v_cvt_pk_bf16_f32 v69, v88, v89
	v_cvt_pk_bf16_f32 v70, v90, v91
	v_cvt_pk_bf16_f32 v71, v92, v93
	v_cvt_pk_bf16_f32 v72, v94, v95
	v_add_u32_e32 v90, s22, v206
	ds_read_b128 v[82:85], v90 offset:53248
	ds_read_b128 v[86:89], v90 offset:58368
	v_cvt_pk_bf16_f32 v74, v210, v211
	v_cvt_pk_bf16_f32 v75, v212, v213
	v_cvt_pk_bf16_f32 v76, v214, v215
	v_cvt_pk_bf16_f32 v77, v216, v217
	v_cvt_pk_bf16_f32 v78, v218, v219
	v_cvt_pk_bf16_f32 v79, v220, v221
	v_cvt_pk_bf16_f32 v80, v222, v223
	v_cvt_pk_bf16_f32 v81, v208, v209
	v_add_u32_e32 v91, 0xd000, v90
	s_waitcnt lgkmcnt(1)
	v_mfma_f32_32x32x16_bf16 v[50:65], v[82:85], v[66:69], v[50:65]
	ds_read_b128 v[82:85], v90 offset:63488
	s_waitcnt lgkmcnt(1)
	v_mfma_f32_32x32x16_bf16 v[34:49], v[86:89], v[66:69], v[34:49]
	ds_read_b128 v[86:89], v91 offset:15360
	s_waitcnt lgkmcnt(1)
	v_mfma_f32_32x32x16_bf16 v[18:33], v[82:85], v[66:69], v[18:33]
	ds_read_b128 v[82:85], v90 offset:53264
	s_waitcnt lgkmcnt(1)
	v_mfma_f32_32x32x16_bf16 v[2:17], v[86:89], v[66:69], v[2:17]
	ds_read_b128 v[66:69], v90 offset:58384
	s_waitcnt lgkmcnt(1)
	v_mfma_f32_32x32x16_bf16 v[50:65], v[82:85], v[70:73], v[50:65]
	ds_read_b128 v[82:85], v90 offset:63504
	s_waitcnt lgkmcnt(1)
	v_mfma_f32_32x32x16_bf16 v[34:49], v[66:69], v[70:73], v[34:49]
	ds_read_b128 v[66:69], v91 offset:15376
	s_waitcnt lgkmcnt(1)
	v_mfma_f32_32x32x16_bf16 v[18:33], v[82:85], v[70:73], v[18:33]
	ds_read_b128 v[82:85], v90 offset:53312
	s_waitcnt lgkmcnt(1)
	v_mfma_f32_32x32x16_bf16 v[2:17], v[66:69], v[70:73], v[2:17]
	ds_read_b128 v[66:69], v90 offset:58432
	s_waitcnt lgkmcnt(1)
	v_mfma_f32_32x32x16_bf16 v[50:65], v[82:85], v[74:77], v[50:65]
	ds_read_b128 v[70:73], v90 offset:63552
	s_waitcnt lgkmcnt(1)
	v_mfma_f32_32x32x16_bf16 v[34:49], v[66:69], v[74:77], v[34:49]
	ds_read_b128 v[66:69], v91 offset:15424
	s_waitcnt lgkmcnt(1)
	v_mfma_f32_32x32x16_bf16 v[18:33], v[70:73], v[74:77], v[18:33]
	ds_read_b128 v[70:73], v90 offset:53328
	s_waitcnt lgkmcnt(1)
	v_mfma_f32_32x32x16_bf16 v[2:17], v[66:69], v[74:77], v[2:17]
	ds_read_b128 v[66:69], v90 offset:58448
	s_waitcnt lgkmcnt(1)
	v_mfma_f32_32x32x16_bf16 v[50:65], v[70:73], v[78:81], v[50:65]
	ds_read_b128 v[70:73], v90 offset:63568
	s_waitcnt lgkmcnt(1)
	v_mfma_f32_32x32x16_bf16 v[34:49], v[66:69], v[78:81], v[34:49]
	ds_read_b128 v[66:69], v91 offset:15440
	s_waitcnt lgkmcnt(1)
	v_mfma_f32_32x32x16_bf16 v[18:33], v[70:73], v[78:81], v[18:33]
	s_waitcnt lgkmcnt(0)
	v_mfma_f32_32x32x16_bf16 v[2:17], v[66:69], v[78:81], v[2:17]
	v_add_f32_e32 v205, v97, v205
	s_andn2_b64 vcc, exec, s[12:13]
	s_cbranch_vccz .LBB0_480
	s_branch .LBB0_481
